# baseline (speedup 1.0000x reference)
.Lw2_keep:
	ds_read_b128 v[162:165], v179 offset:192
	s_waitcnt vmcnt(15) lgkmcnt(5)
	v_mfma_f32_32x32x16_f16 v[30:45], v[98:101], v[26:29], v[30:45]
	ds_read_b128 v[22:25], v179 offset:224
	s_waitcnt vmcnt(14) lgkmcnt(5)
	v_mfma_f32_32x32x16_f16 v[30:45], v[114:117], v[46:49], v[30:45]
	ds_read_b128 v[26:29], v179 offset:256
	s_waitcnt vmcnt(13) lgkmcnt(5)
	v_mfma_f32_32x32x16_f16 v[30:45], v[86:89], v[50:53], v[30:45]
	ds_read_b128 v[46:49], v179 offset:288
	s_waitcnt vmcnt(12) lgkmcnt(5)
	v_mfma_f32_32x32x16_f16 v[30:45], v[126:129], v[54:57], v[30:45]
	ds_read_b128 v[50:53], v179 offset:320
	s_waitcnt vmcnt(11) lgkmcnt(5)
	v_mfma_f32_32x32x16_f16 v[30:45], v[90:93], v[58:61], v[30:45]
	ds_read_b128 v[54:57], v179 offset:352
	s_waitcnt vmcnt(10) lgkmcnt(5)
	v_mfma_f32_32x32x16_f16 v[30:45], v[118:121], v[162:165], v[30:45]
	ds_read_b128 v[58:61], v179 offset:384
	s_waitcnt vmcnt(9) lgkmcnt(5)
	v_mfma_f32_32x32x16_f16 v[30:45], v[78:81], v[22:25], v[30:45]
	ds_read_b128 v[162:165], v179 offset:416
	s_waitcnt vmcnt(8) lgkmcnt(5)
	v_mfma_f32_32x32x16_f16 v[30:45], v[102:105], v[26:29], v[30:45]
	ds_read_b128 v[22:25], v179 offset:448
	s_waitcnt vmcnt(7) lgkmcnt(5)
	v_mfma_f32_32x32x16_f16 v[30:45], v[74:77], v[46:49], v[30:45]
	ds_read_b128 v[26:29], v179 offset:480
	s_waitcnt vmcnt(6) lgkmcnt(5)
	v_mfma_f32_32x32x16_f16 v[30:45], v[106:109], v[50:53], v[30:45]
	s_waitcnt vmcnt(5) lgkmcnt(4)
	v_mfma_f32_32x32x16_f16 v[30:45], v[82:85], v[54:57], v[30:45]
	s_waitcnt vmcnt(4) lgkmcnt(3)
	v_mfma_f32_32x32x16_f16 v[30:45], v[110:113], v[58:61], v[30:45]
	v_pk_add_f16 v48, v18, v146
	v_pk_add_f16 v49, v19, v147
	s_nop 0
	v_pk_mul_f16 v46, v20, v148 clamp
	v_pk_mul_f16 v47, v21, v149 clamp
	v_pk_max_f16 v46, v48, v46
	v_pk_max_f16 v47, v49, v47
	ds_write_b64 v189, v[46:47] offset:33792
	s_waitcnt vmcnt(3) lgkmcnt(3)
	v_mfma_f32_32x32x16_f16 v[30:45], v[94:97], v[162:165], v[30:45]
	v_pk_add_f16 v48, v18, v138
	v_pk_add_f16 v49, v19, v139
	s_nop 0
	v_pk_mul_f16 v46, v20, v140 clamp
	v_pk_mul_f16 v47, v21, v141 clamp
	v_pk_max_f16 v46, v48, v46
	v_pk_max_f16 v47, v49, v47
	ds_write_b64 v189, v[46:47] offset:34320
	s_waitcnt vmcnt(2) lgkmcnt(3)
	v_mfma_f32_32x32x16_f16 v[30:45], v[134:137], v[22:25], v[30:45]
	v_pk_add_f16 v48, v18, v150
	v_pk_add_f16 v49, v19, v151
	s_nop 0
	v_pk_mul_f16 v46, v20, v152 clamp
	v_pk_mul_f16 v47, v21, v153 clamp
	v_pk_max_f16 v46, v48, v46
	v_pk_max_f16 v47, v49, v47
	ds_write_b64 v189, v[46:47] offset:34848
	s_waitcnt vmcnt(1) lgkmcnt(3)
	v_mfma_f32_32x32x16_f16 v[30:45], v[130:133], v[26:29], v[30:45]
	v_pk_add_f16 v22, v18, v142
	v_pk_add_f16 v23, v19, v143
	s_nop 0
	v_pk_mul_f16 v18, v20, v144 clamp
	v_pk_mul_f16 v19, v21, v145 clamp
	v_pk_max_f16 v18, v22, v18
	v_pk_max_f16 v19, v23, v19
	ds_write_b64 v189, v[18:19] offset:35376
	global_load_dwordx4 v[162:165], v[154:155], off
	ds_read_b128 v[46:49], v179 offset:16896
	ds_read_b128 v[50:53], v179 offset:16928
	ds_read_b128 v[54:57], v179 offset:16960
	ds_read_b128 v[58:61], v179 offset:16992
	ds_read_b128 v[168:171], v179 offset:17024
	ds_read_b128 v[172:175], v179 offset:17056
	s_nop 0
	v_cvt_pk_f16_f32 v167, v30, v31
	v_cvt_pk_f16_f32 v177, v32, v33
	s_waitcnt lgkmcnt(5)
	v_mfma_f32_32x32x16_f16 v[18:33], v[122:125], v[46:49], v[2:17]
	ds_read_b128 v[180:183], v179 offset:17088
	s_waitcnt lgkmcnt(5)
	v_mfma_f32_32x32x16_f16 v[18:33], v[98:101], v[50:53], v[18:33]
	ds_read_b128 v[184:187], v179 offset:17120
	v_exp_f16_e64 v46, v167 clamp
	v_exp_f16_e64 v47, v177 clamp
	v_exp_f16_sdwa v46, v167 clamp dst_sel:WORD_1 dst_unused:UNUSED_PRESERVE src0_sel:WORD_1
	v_exp_f16_sdwa v47, v177 clamp dst_sel:WORD_1 dst_unused:UNUSED_PRESERVE src0_sel:WORD_1
	s_nop 0
	s_waitcnt lgkmcnt(5)
	v_mfma_f32_32x32x16_f16 v[18:33], v[114:117], v[54:57], v[18:33]
	ds_read_b128 v[190:193], v179 offset:17152
	s_movk_i32 s0, 0x3dc5
	v_mov_b32_e32 v178, 0xbdc5
	v_pk_fma_f16 v47, v47, s0, v178 op_sel_hi:[1,0,0]
	v_pk_fma_f16 v46, v46, s0, v178 op_sel_hi:[1,0,0]
	v_pk_max_f16 v47, v177, v47
	v_pk_max_f16 v46, v167, v46
	s_waitcnt lgkmcnt(5)
	v_mfma_f32_32x32x16_f16 v[18:33], v[86:89], v[58:61], v[18:33]
	ds_read_b128 v[194:197], v179 offset:17184
	v_cvt_pk_f16_f32 v48, v34, v35
	v_cvt_pk_f16_f32 v49, v36, v37
	s_waitcnt lgkmcnt(5)
	v_mfma_f32_32x32x16_f16 v[18:33], v[126:129], v[168:171], v[18:33]
	ds_read_b128 v[34:37], v179 offset:17216
	v_exp_f16_e64 v50, v48 clamp
	v_exp_f16_e64 v51, v49 clamp
	v_exp_f16_sdwa v50, v48 clamp dst_sel:WORD_1 dst_unused:UNUSED_PRESERVE src0_sel:WORD_1
	v_exp_f16_sdwa v51, v49 clamp dst_sel:WORD_1 dst_unused:UNUSED_PRESERVE src0_sel:WORD_1
	s_nop 0
	s_waitcnt lgkmcnt(5)
	v_mfma_f32_32x32x16_f16 v[18:33], v[90:93], v[172:175], v[18:33]
	ds_read_b128 v[168:171], v179 offset:17248
	v_pk_fma_f16 v51, v51, s0, v178 op_sel_hi:[1,0,0]
	v_pk_fma_f16 v50, v50, s0, v178 op_sel_hi:[1,0,0]
	v_pk_max_f16 v49, v49, v51
	v_pk_max_f16 v48, v48, v50
	s_waitcnt lgkmcnt(5)
	v_mfma_f32_32x32x16_f16 v[18:33], v[118:121], v[180:183], v[18:33]
	ds_read_b128 v[172:175], v179 offset:17280
	v_cvt_pk_f16_f32 v167, v38, v39
	v_cvt_pk_f16_f32 v177, v40, v41
	v_mfma_f32_16x16x32_f16 v[58:61], v[70:73], v[46:49], 0
	s_waitcnt lgkmcnt(5)
	v_mfma_f32_32x32x16_f16 v[18:33], v[78:81], v[184:187], v[18:33]
	ds_read_b128 v[38:41], v179 offset:17312
	v_exp_f16_e64 v188, v167 clamp
	v_exp_f16_e64 v198, v177 clamp
	v_exp_f16_sdwa v188, v167 clamp dst_sel:WORD_1 dst_unused:UNUSED_PRESERVE src0_sel:WORD_1
	v_exp_f16_sdwa v198, v177 clamp dst_sel:WORD_1 dst_unused:UNUSED_PRESERVE src0_sel:WORD_1
	s_nop 0
	s_waitcnt lgkmcnt(5)
	v_mfma_f32_32x32x16_f16 v[18:33], v[102:105], v[190:193], v[18:33]
	ds_read_b128 v[180:183], v179 offset:17344
	v_pk_fma_f16 v184, v198, s0, v178 op_sel_hi:[1,0,0]
	s_nop 0
	v_pk_max_f16 v185, v177, v184
	v_pk_fma_f16 v177, v188, s0, v178 op_sel_hi:[1,0,0]
	s_nop 0
	v_pk_max_f16 v184, v167, v177
	s_waitcnt lgkmcnt(5)
	v_mfma_f32_32x32x16_f16 v[18:33], v[74:77], v[194:197], v[18:33]
	ds_read_b128 v[190:193], v179 offset:17376
	v_cvt_pk_f16_f32 v42, v42, v43
	v_cvt_pk_f16_f32 v43, v44, v45
	s_waitcnt lgkmcnt(5)
	v_mfma_f32_32x32x16_f16 v[18:33], v[106:109], v[34:37], v[18:33]
	v_exp_f16_e64 v44, v42 clamp
	v_exp_f16_e64 v45, v43 clamp
	v_exp_f16_sdwa v44, v42 clamp dst_sel:WORD_1 dst_unused:UNUSED_PRESERVE src0_sel:WORD_1
	v_exp_f16_sdwa v45, v43 clamp dst_sel:WORD_1 dst_unused:UNUSED_PRESERVE src0_sel:WORD_1
	s_nop 0
	s_waitcnt lgkmcnt(4)
	v_mfma_f32_32x32x16_f16 v[18:33], v[82:85], v[168:171], v[18:33]
	v_pk_fma_f16 v34, v45, s0, v178 op_sel_hi:[1,0,0]
	s_nop 0
	v_pk_max_f16 v187, v43, v34
	v_pk_fma_f16 v34, v44, s0, v178 op_sel_hi:[1,0,0]
	s_nop 0
	v_pk_max_f16 v186, v42, v34
	s_waitcnt lgkmcnt(3)
	v_mfma_f32_32x32x16_f16 v[18:33], v[110:113], v[172:175], v[18:33]
	v_pk_add_f16 v36, v62, v146
	v_pk_add_f16 v37, v63, v147
	s_nop 0
	v_pk_mul_f16 v34, v64, v148 clamp
	v_pk_mul_f16 v35, v65, v149 clamp
	v_pk_max_f16 v34, v36, v34
	v_pk_max_f16 v35, v37, v35
	ds_write_b64 v189, v[34:35] offset:50688
	v_mfma_f32_16x16x32_f16 v[58:61], v[66:69], v[184:187], v[58:61]
	s_waitcnt lgkmcnt(3)
	v_mfma_f32_32x32x16_f16 v[18:33], v[94:97], v[38:41], v[18:33]
	v_pk_add_f16 v36, v62, v138
	v_pk_add_f16 v37, v63, v139
	s_nop 0
	v_pk_mul_f16 v34, v64, v140 clamp
	v_pk_mul_f16 v35, v65, v141 clamp
	v_pk_max_f16 v34, v36, v34
	v_pk_max_f16 v35, v37, v35
	ds_write_b64 v189, v[34:35] offset:51216
	s_waitcnt lgkmcnt(3)
	v_mfma_f32_32x32x16_f16 v[18:33], v[134:137], v[180:183], v[18:33]
	v_pk_add_f16 v36, v62, v150
	v_pk_add_f16 v37, v63, v151
	s_nop 0
	v_pk_mul_f16 v34, v64, v152 clamp
	v_pk_mul_f16 v35, v65, v153 clamp
	v_pk_max_f16 v34, v36, v34
	v_pk_max_f16 v35, v37, v35
	ds_write_b64 v189, v[34:35] offset:51744
	s_waitcnt lgkmcnt(3)
	v_mfma_f32_32x32x16_f16 v[18:33], v[130:133], v[190:193], v[18:33]
	v_pk_add_f16 v36, v62, v142
	v_pk_add_f16 v37, v63, v143
	s_nop 0
	v_pk_mul_f16 v34, v64, v144 clamp
	v_pk_mul_f16 v35, v65, v145 clamp
	v_pk_max_f16 v34, v36, v34
	v_pk_max_f16 v35, v37, v35
	ds_write_b64 v189, v[34:35] offset:52272
	v_and_b32_e32 v157, 15, v199
	v_lshrrev_b32_e32 v1, 5, v199
	v_lshl_or_b32 v157, v1, 4, v157
	v_bfe_u32 v1, v199, 4, 1
	v_lshlrev_b32_e32 v1, 2, v1
	v_or_b32_e32 v178, s2, v157
	v_mul_lo_u32 v167, v178, 7
	v_add_u32_e32 v170, v167, v1
	v_mov_b32_e32 v34, 0x10800
	v_lshl_add_u32 v206, v170, 2, v34
	v_and_b32_e32 v34, 16, v199
	v_cmp_eq_u32_e64 s[0:1], 0, v34
	v_mov_b32_e32 v34, 0x10808
	v_lshl_add_u32 v34, v167, 2, v34
	v_or_b32_e32 v36, 3, v1
	v_mul_i32_i24_e32 v34, -6, v156
	v_mul_u32_u24_e32 v35, 7, v156
	v_cmp_gt_u32_e64 s[2:3], 6, v36
	v_lshlrev_b32_e32 v171, 2, v167
	v_lshlrev_b32_e32 v172, 2, v36
	s_mov_b32 s5, 0x10800
	v_add3_u32 v36, v171, v172, s5
	ds_write2_b32 v206, v58, v59 offset1:1
	s_and_saveexec_b64 s[2:3], s[0:1]
	ds_write2_b32 v206, v60, v61 offset0:2 offset1:3
	s_or_b64 exec, exec, s[2:3]
	s_sub_i32 s9, 0xff, s28
	s_mul_i32 s9, s9, s28
	s_not_b32 s25, s28
	s_ashr_i32 s9, s9, 1
	s_add_i32 s24, s24, s25
	s_add_i32 s24, s24, s9
	s_mul_i32 s8, s39, 0x1fc0
	s_ashr_i32 s9, s24, 31
	s_mul_hi_u32 s5, s39, 0x1fc0
	s_add_u32 s8, s8, s24
	s_addc_u32 s5, s5, s9
	s_mul_i32 s5, s5, 6
	s_mul_hi_u32 s9, s8, 6
	s_add_i32 s9, s9, s5
	v_add_u32_e32 v34, v34, v0
	s_cmpk_lt_u32 s21, 0xc0
	v_add_u32_e32 v173, v34, v35
	v_lshl_or_b32 v177, v34, 8, v156
	s_mul_i32 s8, s8, 6
	s_cselect_b64 s[24:25], -1, 0
	s_cmpk_gt_u32 s21, 0xbf
	s_waitcnt lgkmcnt(0)
	s_barrier
	s_cbranch_scc1 .LBB1_33
	s_andn2_b64 vcc, exec, s[6:7]
	s_mov_b64 s[6:7], -1
	s_cbranch_vccnz .LBB1_29
	s_movk_i32 s5, 0x60
	v_cmp_gt_u32_e32 vcc, s5, v0
	s_and_saveexec_b64 s[6:7], vcc
	s_cbranch_execz .LBB1_28
	v_lshlrev_b32_e32 v38, 2, v173
	v_add_u32_e32 v46, 0x10800, v38
	ds_read2_b32 v[34:35], v46 offset1:224
	v_add_u32_e32 v36, 0x700, v46
	ds_read2_b32 v[36:37], v36 offset1:224
	v_add_u32_e32 v38, 0xe00, v46
	ds_read2_b32 v[38:39], v38 offset1:224
	v_add_u32_e32 v40, 0x1500, v46
	ds_read2_b32 v[40:41], v40 offset1:224
	s_lshl_b64 s[26:27], s[8:9], 2
	s_add_u32 s26, s10, s26
	s_addc_u32 s27, s11, s27
	s_waitcnt lgkmcnt(3)
	v_add_f32_e32 v34, 0, v34
	v_add_f32_e32 v34, v34, v35
	s_waitcnt lgkmcnt(2)
	v_add_f32_e32 v34, v34, v36
	v_add_f32_e32 v34, v34, v37
	s_waitcnt lgkmcnt(1)
	v_add_f32_e32 v34, v34, v38
	v_add_f32_e32 v34, v34, v39
	s_waitcnt lgkmcnt(0)
	v_add_f32_e32 v34, v34, v40
	v_add_f32_e32 v34, v34, v41
	v_fmamk_f32 v34, v34, 0x3eb17218, v176
	v_lshlrev_b32 v35, 2, v0
	global_store_dword v35, v34, s[26:27]

.LBB1_46:
.LBB1_47:
	s_and_saveexec_b64 s[28:29], s[4:5]
	s_cbranch_execz .LBB1_49
	ds_read2_b32 v[34:35], v200 offset1:224
	ds_read2_b32 v[36:37], v234 offset1:224
	ds_read2_b32 v[38:39], v235 offset1:224
	ds_read2_b32 v[40:41], v236 offset1:224
	s_lshl_b64 s[34:35], s[26:27], 2
	s_add_u32 s34, s10, s34
	s_addc_u32 s35, s11, s35
	s_waitcnt lgkmcnt(3)
	v_add_f32_e32 v34, 0, v34
	v_add_f32_e32 v34, v34, v35
	s_waitcnt lgkmcnt(2)
	v_add_f32_e32 v34, v34, v36
	v_add_f32_e32 v34, v34, v37
	s_waitcnt lgkmcnt(1)
	v_add_f32_e32 v34, v34, v38
	v_add_f32_e32 v34, v34, v39
	s_waitcnt lgkmcnt(0)
	v_add_f32_e32 v34, v34, v40
	v_add_f32_e32 v34, v34, v41
	v_fmamk_f32 v34, v34, 0x3eb17218, v176
	v_lshlrev_b32 v35, 2, v0
	global_store_dword v35, v34, s[34:35]

.LBB1_55:
.LBB1_56:
	s_and_saveexec_b64 s[28:29], s[4:5]
	s_cbranch_execz .LBB1_58
	ds_read2_b32 v[34:35], v190 offset1:224
	ds_read2_b32 v[36:37], v237 offset1:224
	ds_read2_b32 v[38:39], v238 offset1:224
	ds_read2_b32 v[40:41], v239 offset1:224
	s_lshl_b64 s[34:35], s[26:27], 2
	s_add_u32 s34, s10, s34
	s_addc_u32 s35, s11, s35
	s_waitcnt lgkmcnt(3)
	v_add_f32_e32 v34, 0, v34
	v_add_f32_e32 v34, v34, v35
	s_waitcnt lgkmcnt(2)
	v_add_f32_e32 v34, v34, v36
	v_add_f32_e32 v34, v34, v37
	s_waitcnt lgkmcnt(1)
	v_add_f32_e32 v34, v34, v38
	v_add_f32_e32 v34, v34, v39
	s_waitcnt lgkmcnt(0)
	v_add_f32_e32 v34, v34, v40
	v_add_f32_e32 v34, v34, v41
	v_fmamk_f32 v34, v34, 0x3eb17218, v176
	v_lshlrev_b32 v35, 2, v0
	global_store_dword v35, v34, s[34:35]

.LBB1_72:
.LBB1_73:
	s_and_saveexec_b64 s[28:29], s[4:5]
	s_cbranch_execz .LBB1_75
	ds_read2_b32 v[34:35], v180 offset1:224
	v_add_u32_e32 v36, 0x700, v180
	ds_read2_b32 v[36:37], v36 offset1:224
	v_add_u32_e32 v38, 0xe00, v180
	ds_read2_b32 v[38:39], v38 offset1:224
	v_add_u32_e32 v40, 0x1500, v180
	ds_read2_b32 v[40:41], v40 offset1:224
	s_lshl_b64 s[34:35], s[26:27], 2
	s_add_u32 s34, s10, s34
	s_addc_u32 s35, s11, s35
	s_waitcnt lgkmcnt(3)
	v_add_f32_e32 v34, 0, v34
	v_add_f32_e32 v34, v34, v35
	s_waitcnt lgkmcnt(2)
	v_add_f32_e32 v34, v34, v36
	v_add_f32_e32 v34, v34, v37
	s_waitcnt lgkmcnt(1)
	v_add_f32_e32 v34, v34, v38
	v_add_f32_e32 v34, v34, v39
	s_waitcnt lgkmcnt(0)
	v_add_f32_e32 v34, v34, v40
	v_add_f32_e32 v34, v34, v41
	v_fmamk_f32 v34, v34, 0x3eb17218, v176
	v_lshlrev_b32 v35, 2, v0
	global_store_dword v35, v34, s[34:35]

.LBB1_81:
.LBB1_82:
	s_and_saveexec_b64 s[26:27], s[4:5]
	s_cbranch_execz .LBB1_84
	ds_read2_b32 v[34:35], v216 offset1:224
	v_add_u32_e32 v36, 0x700, v216
	ds_read2_b32 v[36:37], v36 offset1:224
	v_add_u32_e32 v38, 0xe00, v216
	ds_read2_b32 v[38:39], v38 offset1:224
	v_add_u32_e32 v40, 0x1500, v216
	ds_read2_b32 v[40:41], v40 offset1:224
	s_lshl_b64 s[30:31], s[28:29], 2
	s_add_u32 s30, s10, s30
	s_addc_u32 s31, s11, s31
	s_waitcnt lgkmcnt(3)
	v_add_f32_e32 v34, 0, v34
	v_add_f32_e32 v34, v34, v35
	s_waitcnt lgkmcnt(2)
	v_add_f32_e32 v34, v34, v36
	v_add_f32_e32 v34, v34, v37
	s_waitcnt lgkmcnt(1)
	v_add_f32_e32 v34, v34, v38
	v_add_f32_e32 v34, v34, v39
	s_waitcnt lgkmcnt(0)
	v_add_f32_e32 v34, v34, v40
	v_add_f32_e32 v34, v34, v41
	v_fmamk_f32 v34, v34, 0x3eb17218, v176
	v_lshlrev_b32 v35, 2, v0
	global_store_dword v35, v34, s[30:31]

.LBB1_106:
.LBB1_107:
	s_and_saveexec_b64 s[30:31], s[4:5]
	s_cbranch_execz .LBB1_109
	ds_read2_b32 v[34:35], v200 offset1:224
	ds_read2_b32 v[36:37], v234 offset1:224
	ds_read2_b32 v[38:39], v235 offset1:224
	ds_read2_b32 v[40:41], v236 offset1:224
	s_lshl_b64 s[36:37], s[28:29], 2
	s_add_u32 s36, s10, s36
	s_addc_u32 s37, s11, s37
	s_waitcnt lgkmcnt(3)
	v_add_f32_e32 v34, 0, v34
	v_add_f32_e32 v34, v34, v35
	s_waitcnt lgkmcnt(2)
	v_add_f32_e32 v34, v34, v36
	v_add_f32_e32 v34, v34, v37
	s_waitcnt lgkmcnt(1)
	v_add_f32_e32 v34, v34, v38
	v_add_f32_e32 v34, v34, v39
	s_waitcnt lgkmcnt(0)
	v_add_f32_e32 v34, v34, v40
	v_add_f32_e32 v34, v34, v41
	v_fmamk_f32 v34, v34, 0x3eb17218, v176
	v_lshlrev_b32 v35, 2, v0
	global_store_dword v35, v34, s[36:37]

.LBB1_115:
.LBB1_116:
	s_and_saveexec_b64 s[30:31], s[4:5]
	s_cbranch_execz .LBB1_118
	ds_read2_b32 v[34:35], v190 offset1:224
	ds_read2_b32 v[36:37], v237 offset1:224
	ds_read2_b32 v[38:39], v238 offset1:224
	ds_read2_b32 v[40:41], v239 offset1:224
	s_lshl_b64 s[36:37], s[28:29], 2
	s_add_u32 s36, s10, s36
	s_addc_u32 s37, s11, s37
	s_waitcnt lgkmcnt(3)
	v_add_f32_e32 v34, 0, v34
	v_add_f32_e32 v34, v34, v35
	s_waitcnt lgkmcnt(2)
	v_add_f32_e32 v34, v34, v36
	v_add_f32_e32 v34, v34, v37
	s_waitcnt lgkmcnt(1)
	v_add_f32_e32 v34, v34, v38
	v_add_f32_e32 v34, v34, v39
	s_waitcnt lgkmcnt(0)
	v_add_f32_e32 v34, v34, v40
	v_add_f32_e32 v34, v34, v41
	v_fmamk_f32 v34, v34, 0x3eb17218, v176
	v_lshlrev_b32 v35, 2, v0
	global_store_dword v35, v34, s[36:37]

.LBB1_132:
.LBB1_133:
	s_and_saveexec_b64 s[30:31], s[4:5]
	s_cbranch_execz .LBB1_135
	ds_read2_b32 v[34:35], v180 offset1:224
	v_add_u32_e32 v36, 0x700, v180
	ds_read2_b32 v[36:37], v36 offset1:224
	v_add_u32_e32 v38, 0xe00, v180
	ds_read2_b32 v[38:39], v38 offset1:224
	v_add_u32_e32 v40, 0x1500, v180
	ds_read2_b32 v[40:41], v40 offset1:224
	s_lshl_b64 s[36:37], s[28:29], 2
	s_add_u32 s36, s10, s36
	s_addc_u32 s37, s11, s37
	s_waitcnt lgkmcnt(3)
	v_add_f32_e32 v34, 0, v34
	v_add_f32_e32 v34, v34, v35
	s_waitcnt lgkmcnt(2)
	v_add_f32_e32 v34, v34, v36
	v_add_f32_e32 v34, v34, v37
	s_waitcnt lgkmcnt(1)
	v_add_f32_e32 v34, v34, v38
	v_add_f32_e32 v34, v34, v39
	s_waitcnt lgkmcnt(0)
	v_add_f32_e32 v34, v34, v40
	v_add_f32_e32 v34, v34, v41
	v_fmamk_f32 v34, v34, 0x3eb17218, v176
	v_lshlrev_b32 v35, 2, v0
	global_store_dword v35, v34, s[36:37]

.LBB1_141:
.LBB1_142:
	s_and_saveexec_b64 s[30:31], s[4:5]
	s_cbranch_execz .LBB1_144
	ds_read2_b32 v[34:35], v216 offset1:224
	v_add_u32_e32 v36, 0x700, v216
	ds_read2_b32 v[36:37], v36 offset1:224
	v_add_u32_e32 v38, 0xe00, v216
	ds_read2_b32 v[38:39], v38 offset1:224
	v_add_u32_e32 v40, 0x1500, v216
	ds_read2_b32 v[40:41], v40 offset1:224
	s_lshl_b64 s[36:37], s[28:29], 2
	s_add_u32 s36, s10, s36
	s_addc_u32 s37, s11, s37
	s_waitcnt lgkmcnt(3)
	v_add_f32_e32 v34, 0, v34
	v_add_f32_e32 v34, v34, v35
	s_waitcnt lgkmcnt(2)
	v_add_f32_e32 v34, v34, v36
	v_add_f32_e32 v34, v34, v37
	s_waitcnt lgkmcnt(1)
	v_add_f32_e32 v34, v34, v38
	v_add_f32_e32 v34, v34, v39
	s_waitcnt lgkmcnt(0)
	v_add_f32_e32 v34, v34, v40
	v_add_f32_e32 v34, v34, v41
	v_fmamk_f32 v34, v34, 0x3eb17218, v176
	v_lshlrev_b32 v35, 2, v0
	global_store_dword v35, v34, s[36:37]

.LBB1_160:
.LBB1_161:
	s_and_saveexec_b64 s[12:13], s[4:5]
	s_cbranch_execz .LBB1_163
	ds_read2_b32 v[34:35], v200 offset1:224
	v_add_u32_e32 v36, 0x700, v200
	ds_read2_b32 v[36:37], v36 offset1:224
	v_add_u32_e32 v38, 0xe00, v200
	ds_read2_b32 v[38:39], v38 offset1:224
	v_add_u32_e32 v40, 0x1500, v200
	ds_read2_b32 v[40:41], v40 offset1:224
	s_lshl_b64 s[20:21], s[26:27], 2
	s_add_u32 s20, s10, s20
	s_addc_u32 s21, s11, s21
	s_waitcnt lgkmcnt(3)
	v_add_f32_e32 v34, 0, v34
	v_add_f32_e32 v34, v34, v35
	s_waitcnt lgkmcnt(2)
	v_add_f32_e32 v34, v34, v36
	v_add_f32_e32 v34, v34, v37
	s_waitcnt lgkmcnt(1)
	v_add_f32_e32 v34, v34, v38
	v_add_f32_e32 v34, v34, v39
	s_waitcnt lgkmcnt(0)
	v_add_f32_e32 v34, v34, v40
	v_add_f32_e32 v34, v34, v41
	v_fmamk_f32 v34, v34, 0x3eb17218, v176
	v_lshlrev_b32 v35, 2, v0
	global_store_dword v35, v34, s[20:21]

.LBB1_169:
.LBB1_170:
	s_and_saveexec_b64 s[20:21], s[4:5]
	s_cbranch_execz .LBB1_172
	ds_read2_b32 v[34:35], v190 offset1:224
	v_add_u32_e32 v36, 0x700, v190
	ds_read2_b32 v[36:37], v36 offset1:224
	v_add_u32_e32 v38, 0xe00, v190
	ds_read2_b32 v[38:39], v38 offset1:224
	v_add_u32_e32 v40, 0x1500, v190
	ds_read2_b32 v[40:41], v40 offset1:224
	s_lshl_b64 s[22:23], s[12:13], 2
	s_add_u32 s22, s10, s22
	s_addc_u32 s23, s11, s23
	s_waitcnt lgkmcnt(3)
	v_add_f32_e32 v34, 0, v34
	v_add_f32_e32 v34, v34, v35
	s_waitcnt lgkmcnt(2)
	v_add_f32_e32 v34, v34, v36
	v_add_f32_e32 v34, v34, v37
	s_waitcnt lgkmcnt(1)
	v_add_f32_e32 v34, v34, v38
	v_add_f32_e32 v34, v34, v39
	s_waitcnt lgkmcnt(0)
	v_add_f32_e32 v34, v34, v40
	v_add_f32_e32 v34, v34, v41
	v_fmamk_f32 v34, v34, 0x3eb17218, v176
	v_lshlrev_b32 v35, 2, v0
	global_store_dword v35, v34, s[22:23]

.LBB1_186:
.LBB1_187:
	s_and_saveexec_b64 s[20:21], s[4:5]
	s_cbranch_execz .LBB1_189
	ds_read2_b32 v[34:35], v180 offset1:224
	v_add_u32_e32 v36, 0x700, v180
	ds_read2_b32 v[36:37], v36 offset1:224
	v_add_u32_e32 v38, 0xe00, v180
	ds_read2_b32 v[38:39], v38 offset1:224
	v_add_u32_e32 v40, 0x1500, v180
	ds_read2_b32 v[40:41], v40 offset1:224
	s_lshl_b64 s[22:23], s[12:13], 2
	s_add_u32 s22, s10, s22
	s_addc_u32 s23, s11, s23
	s_waitcnt lgkmcnt(3)
	v_add_f32_e32 v34, 0, v34
	v_add_f32_e32 v34, v34, v35
	s_waitcnt lgkmcnt(2)
	v_add_f32_e32 v34, v34, v36
	v_add_f32_e32 v34, v34, v37
	s_waitcnt lgkmcnt(1)
	v_add_f32_e32 v34, v34, v38
	v_add_f32_e32 v34, v34, v39
	s_waitcnt lgkmcnt(0)
	v_add_f32_e32 v34, v34, v40
	v_add_f32_e32 v34, v34, v41
	v_fmamk_f32 v34, v34, 0x3eb17218, v176
	v_lshlrev_b32 v35, 2, v0
	global_store_dword v35, v34, s[22:23]

.LBB1_195:
.LBB1_196:
	s_and_saveexec_b64 s[20:21], s[4:5]
	s_cbranch_execz .LBB1_198
	ds_read2_b32 v[34:35], v216 offset1:224
	v_add_u32_e32 v36, 0x700, v216
	ds_read2_b32 v[36:37], v36 offset1:224
	v_add_u32_e32 v38, 0xe00, v216
	ds_read2_b32 v[38:39], v38 offset1:224
	v_add_u32_e32 v40, 0x1500, v216
	ds_read2_b32 v[40:41], v40 offset1:224
	s_lshl_b64 s[22:23], s[12:13], 2
	s_add_u32 s22, s10, s22
	s_addc_u32 s23, s11, s23
	s_waitcnt lgkmcnt(3)
	v_add_f32_e32 v34, 0, v34
	v_add_f32_e32 v34, v34, v35
	s_waitcnt lgkmcnt(2)
	v_add_f32_e32 v34, v34, v36
	v_add_f32_e32 v34, v34, v37
	s_waitcnt lgkmcnt(1)
	v_add_f32_e32 v34, v34, v38
	v_add_f32_e32 v34, v34, v39
	s_waitcnt lgkmcnt(0)
	v_add_f32_e32 v34, v34, v40
	v_add_f32_e32 v34, v34, v41
	v_fmamk_f32 v34, v34, 0x3eb17218, v176
	v_lshlrev_b32 v35, 2, v0
	global_store_dword v35, v34, s[22:23]

.LBB1_212:
.LBB1_213:
	s_and_saveexec_b64 s[20:21], s[4:5]
	s_cbranch_execz .LBB1_215
	ds_read2_b32 v[18:19], v200 offset1:224
	v_add_u32_e32 v20, 0x700, v200
	ds_read2_b32 v[20:21], v20 offset1:224
	v_add_u32_e32 v22, 0xe00, v200
	ds_read2_b32 v[22:23], v22 offset1:224
	v_add_u32_e32 v24, 0x1500, v200
	ds_read2_b32 v[24:25], v24 offset1:224
	s_lshl_b64 s[22:23], s[12:13], 2
	s_add_u32 s22, s10, s22
	s_addc_u32 s23, s11, s23
	s_waitcnt lgkmcnt(3)
	v_add_f32_e32 v18, 0, v18
	v_add_f32_e32 v18, v18, v19
	s_waitcnt lgkmcnt(2)
	v_add_f32_e32 v18, v18, v20
	v_add_f32_e32 v18, v18, v21
	s_waitcnt lgkmcnt(1)
	v_add_f32_e32 v18, v18, v22
	v_add_f32_e32 v18, v18, v23
	s_waitcnt lgkmcnt(0)
	v_add_f32_e32 v18, v18, v24
	v_add_f32_e32 v18, v18, v25
	v_fmamk_f32 v18, v18, 0x3eb17218, v176
	v_lshlrev_b32 v19, 2, v0
	global_store_dword v19, v18, s[22:23]

.LBB1_221:
.LBB1_222:
	s_and_saveexec_b64 s[20:21], s[4:5]
	s_cbranch_execz .LBB1_224
	ds_read2_b32 v[18:19], v190 offset1:224
	v_add_u32_e32 v20, 0x700, v190
	ds_read2_b32 v[20:21], v20 offset1:224
	v_add_u32_e32 v22, 0xe00, v190
	ds_read2_b32 v[22:23], v22 offset1:224
	v_add_u32_e32 v24, 0x1500, v190
	ds_read2_b32 v[24:25], v24 offset1:224
	s_lshl_b64 s[22:23], s[12:13], 2
	s_add_u32 s22, s10, s22
	s_addc_u32 s23, s11, s23
	s_waitcnt lgkmcnt(3)
	v_add_f32_e32 v18, 0, v18
	v_add_f32_e32 v18, v18, v19
	s_waitcnt lgkmcnt(2)
	v_add_f32_e32 v18, v18, v20
	v_add_f32_e32 v18, v18, v21
	s_waitcnt lgkmcnt(1)
	v_add_f32_e32 v18, v18, v22
	v_add_f32_e32 v18, v18, v23
	s_waitcnt lgkmcnt(0)
	v_add_f32_e32 v18, v18, v24
	v_add_f32_e32 v18, v18, v25
	v_fmamk_f32 v18, v18, 0x3eb17218, v176
	v_lshlrev_b32 v19, 2, v0
	global_store_dword v19, v18, s[22:23]

.LBB1_237:
.LBB1_238:
	s_and_saveexec_b64 s[0:1], s[4:5]
	s_cbranch_execz .LBB1_240
	ds_read2_b32 v[2:3], v180 offset1:224
	v_add_u32_e32 v4, 0x700, v180
	ds_read2_b32 v[4:5], v4 offset1:224
	v_add_u32_e32 v6, 0xe00, v180
	ds_read2_b32 v[6:7], v6 offset1:224
	v_add_u32_e32 v8, 0x1500, v180
	ds_read2_b32 v[8:9], v8 offset1:224
	s_sub_i32 s2, 0x78, s30
	s_mul_i32 s2, s2, 6
	s_ashr_i32 s3, s2, 31
	s_lshl_b64 s[4:5], s[12:13], 2
	s_add_u32 s4, s10, s4
	s_addc_u32 s5, s11, s5
	s_lshl_b64 s[2:3], s[2:3], 2
	s_add_u32 s2, s4, s2
	s_addc_u32 s3, s5, s3
	s_waitcnt lgkmcnt(3)
	v_add_f32_e32 v1, 0, v2
	v_add_f32_e32 v1, v1, v3
	s_waitcnt lgkmcnt(2)
	v_add_f32_e32 v1, v1, v4
	v_add_f32_e32 v1, v1, v5
	s_waitcnt lgkmcnt(1)
	v_add_f32_e32 v1, v1, v6
	v_add_f32_e32 v1, v1, v7
	s_waitcnt lgkmcnt(0)
	v_add_f32_e32 v1, v1, v8
	v_add_f32_e32 v1, v1, v9
	v_fmamk_f32 v1, v1, 0x3eb17218, v176
	v_lshlrev_b32 v2, 2, v0
	global_store_dword v2, v1, s[2:3]
